# v58 + moe1 unit loop: next unit's row-scale lookup chain (liste -> RS) started at the top of the unit and landed during the K-loop
# baseline (speedup 1.0000x reference)
; #define LAS __attribute__((address_space(3)))
; #define PG8_AOFFS(dst, U) do { int t2_ = tid; asm volatile("" : "+v"(t2_)); _Pragma("unroll") for (int i = 0; i < 2; ++i) { int R, C; stage_rc(t2_ * 16 + i * 8192, R, C); \
;         dst[0][i] = S.a_off(U, R) + (unsigned)C * 2u; dst[1][i] = S.a_off(U, HALF + R) + (unsigned)C * 2u; } } while (0)
;     __device__ __forceinline__ bool next(int i, Unit& u) const { return o.next(i, u); }
; template <class Epi, class Sched>
; __device__ __forceinline__ void gemm_phase(LAS unsigned char* lds, const int tid, const char* Abase, const int K, const Sched& S, const Epi& E) {
;     ...
;         const bool has_next = S.next(ui + 1, nxt);
;         const char* nB = cB;
;         { unsigned vn[2][2];
;           if (has_next) { PG8_AOFFS(vn, nxt); nB = S.b_tile(nxt); *vslot = (u32x4){vn[0][0], vn[0][1], vn[1][0], vn[1][1]}; }
;     EPI_NOMID
;     __device__ __forceinline__ void begin(const Unit& u, int ui, int tid, LAS unsigned char* lds) const {
;         if (tid < 256) { float rs = 0.f; if (tid < u.nrows) rs = RS[liste[(size_t)u.e * T + 256 * u.tile + tid] >> 1]; rtab_put(lds, ui, tid, rs, 0.f); } }
.LBB0_1175:
	v_cndmask_b32_e64 v0, 0, 1, s[38:39]
	s_xor_b64 s[36:37], s[38:39], -1
	v_cmp_ne_u32_e64 s[12:13], 1, v0
	s_andn2_b64 vcc, exec, s[38:39]
	s_mov_b64 s[38:39], s[40:41]
	s_waitcnt lgkmcnt(0)
	v_mov_b32_e32 v137, v5
	v_mov_b32_e32 v136, v4
	v_mov_b32_e32 v135, v3
	v_mov_b32_e32 v134, v2
	s_cbranch_vccnz .LBB0_1185
	v_mov_b32_e32 v136, v188
	s_ashr_i32 s35, s34, 31
	v_ashrrev_i32_e32 v0, 31, v136
	v_lshrrev_b32_e32 v0, 26, v0
	v_lshlrev_b32_e32 v146, 4, v136
	v_add_u32_e32 v0, v136, v0
	v_bfe_i32 v136, v136, 27, 1
	v_lshrrev_b32_e32 v136, 22, v136
	v_add_u32_e32 v136, v146, v136
	v_and_b32_e32 v136, 0xfffffc00, v136
	v_sub_u32_e32 v136, v146, v136
	v_lshrrev_b32_e32 v137, 4, v136
	v_bitop3_b32 v142, v137, v136, 32 bitop3:0x6c
	v_ashrrev_i32_e32 v137, 31, v142
	v_ashrrev_i32_e32 v0, 6, v0
	v_lshrrev_b32_e32 v137, 26, v137
	v_lshlrev_b32_e32 v134, 8, v158
	s_lshl_b64 s[6:7], s[34:35], 17
	v_lshlrev_b32_e32 v136, 3, v0
	v_add_u32_e32 v137, v142, v137
	v_ashrrev_i32_e32 v135, 31, v134
	s_add_u32 s6, s2, s6
	v_and_b32_e32 v136, -16, v136
	v_ashrrev_i32_e32 v143, 6, v137
	s_addc_u32 s7, s33, s7
	v_lshlrev_b64 v[134:135], 2, v[134:135]
	v_add_u32_e32 v136, v143, v136
	v_lshl_add_u64 v[134:135], s[6:7], 0, v[134:135]
	v_mov_b32_e32 v244, 0
	v_mov_b32_e32 v245, 0
	v_cmp_lt_i32_e32 vcc, v188, v157
	s_and_b64 vcc, vcc, s[10:11]
	s_and_saveexec_b64 s[38:39], vcc
	v_lshl_add_u64 v[246:247], v[188:189], 2, v[134:135]
	flat_load_dword v244, v[246:247]
	s_or_b64 exec, exec, s[38:39]
	v_cmp_lt_i32_e32 vcc, v136, v157
	v_mov_b32_e32 v144, 0
	v_ashrrev_i32_e32 v137, 31, v136
	v_mov_b32_e32 v145, 0
	s_and_saveexec_b64 s[38:39], vcc
	s_cbranch_execz .LBB0_1178
	v_lshl_add_u64 v[148:149], v[136:137], 2, v[134:135]
	flat_load_dword v145, v[148:149]

; #define LAS __attribute__((address_space(3)))
; #define PG8_AOFFS(dst, U) do { int t2_ = tid; asm volatile("" : "+v"(t2_)); _Pragma("unroll") for (int i = 0; i < 2; ++i) { int R, C; stage_rc(t2_ * 16 + i * 8192, R, C); \
;         dst[0][i] = S.a_off(U, R) + (unsigned)C * 2u; dst[1][i] = S.a_off(U, HALF + R) + (unsigned)C * 2u; } } while (0)
; template <class Epi, class Sched>
; __device__ __forceinline__ void gemm_phase(LAS unsigned char* lds, const int tid, const char* Abase, const int K, const Sched& S, const Epi& E) {
;     ...
;           if (has_next) { PG8_AOFFS(vn, nxt); nB = S.b_tile(nxt); *vslot = (u32x4){vn[0][0], vn[0][1], vn[1][0], vn[1][1]}; }
;     EPI_NOMID
;     __device__ __forceinline__ void begin(const Unit& u, int ui, int tid, LAS unsigned char* lds) const {
;         if (tid < 256) { float rs = 0.f; if (tid < u.nrows) rs = RS[liste[(size_t)u.e * T + 256 * u.tile + tid] >> 1]; rtab_put(lds, ui, tid, rs, 0.f); } }
.LBB0_1184:
	s_or_b64 exec, exec, s[38:39]
	s_waitcnt vmcnt(0) lgkmcnt(0)
	v_lshlrev_b32_e32 v145, 10, v145
	v_lshlrev_b32_e32 v240, 10, v240
	v_lshlrev_b32_e32 v150, 10, v150
	v_lshlrev_b32_e32 v241, 10, v241
	v_and_b32_e32 v145, 0xfffff800, v145
	v_and_b32_e32 v144, 0xfffff800, v240
	v_and_b32_e32 v150, 0xfffff800, v150
	v_and_b32_e32 v148, 0xfffff800, v241
	v_cmp_lt_i32_e32 vcc, v188, v157
	s_and_b64 vcc, vcc, s[10:11]
	s_and_saveexec_b64 s[38:39], vcc
	v_ashrrev_i32_e32 v246, 1, v244
	v_ashrrev_i32_e32 v247, 31, v246
	v_lshl_add_u64 v[246:247], v[246:247], 2, s[14:15]
	flat_load_dword v245, v[246:247]
	s_or_b64 exec, exec, s[38:39]
	v_lshlrev_b32_e32 v135, 6, v149
	v_sub_u32_e32 v135, v147, v135
	v_lshlrev_b32_e32 v134, 5, v146
	v_ashrrev_i16_sdwa v135, v235, sext(v135) dst_sel:DWORD dst_unused:UNUSED_PAD src0_sel:DWORD src1_sel:BYTE_0
	v_and_b32_e32 v134, 32, v134
	v_bfe_i32 v135, v135, 0, 16
	v_add_lshl_u32 v137, v134, v135, 1
	v_lshlrev_b32_e32 v134, 6, v143
	s_ashr_i32 s31, s30, 31
	v_sub_u32_e32 v134, v142, v134
	s_lshl_b64 s[6:7], s[30:31], 19
	s_lshl_b64 s[38:39], s[34:35], 20
	v_lshlrev_b32_e32 v0, 5, v0
	v_ashrrev_i16_sdwa v134, v235, sext(v134) dst_sel:DWORD dst_unused:UNUSED_PAD src0_sel:DWORD src1_sel:BYTE_0
	s_add_u32 s3, s46, s38
	v_and_b32_e32 v0, 32, v0
	v_bfe_i32 v134, v134, 0, 16
	s_addc_u32 s31, s47, s39
	v_add_lshl_u32 v0, v0, v134, 1
	s_add_u32 s38, s3, s6
	v_add_u32_e32 v135, v150, v137
	v_add_u32_e32 v136, v144, v0
	v_add_u32_e32 v134, v145, v0
	v_add_u32_e32 v137, v148, v137
	s_addc_u32 s39, s31, s7

; #define LAS __attribute__((address_space(3)))
; template <class Epi, class Sched>
; __device__ __forceinline__ void gemm_phase(LAS unsigned char* lds, const int tid, const char* Abase, const int K, const Sched& S, const Epi& E) {
;     ...
;         cur = nxt; cB = nB; ++ui;
;         E.begin(cur, ui, tid, lds);
;     EPI_NOMID
;     __device__ __forceinline__ void begin(const Unit& u, int ui, int tid, LAS unsigned char* lds) const {
;         if (tid < 256) { float rs = 0.f; if (tid < u.nrows) rs = RS[liste[(size_t)u.e * T + 256 * u.tile + tid] >> 1]; rtab_put(lds, ui, tid, rs, 0.f); } }
.LBB0_1207:
	s_or_b64 exec, exec, s[40:41]
	s_add_u32 s40, s31, 0xffffff00
	s_addc_u32 s41, s35, -1
	s_and_b64 vcc, exec, s[12:13]
	s_cbranch_vccnz .LBB0_1157
	s_and_saveexec_b64 s[12:13], s[10:11]
	s_cbranch_execz .LBB0_1212
	v_cmp_lt_i32_e32 vcc, v188, v157
	v_mov_b32_e32 v0, 0
	s_and_saveexec_b64 s[16:17], vcc
	s_cbranch_execz .LBB0_1211
	s_ashr_i32 s35, s34, 31
	v_lshlrev_b32_e32 v2, 8, v158
	s_lshl_b64 s[6:7], s[34:35], 17
	v_ashrrev_i32_e32 v3, 31, v2
	s_add_u32 s6, s2, s6
	s_addc_u32 s7, s33, s7
	v_lshlrev_b64 v[2:3], 2, v[2:3]
	v_lshl_add_u64 v[2:3], s[6:7], 0, v[2:3]
	s_waitcnt vmcnt(0)
	v_mov_b32_e32 v0, v245
